# v46 + combine phase: both expert rows of a token fetched together (second row's loads no longer serialized behind the first row's waits)
# speedup vs baseline: 1.0213x; 1.0014x over previous
.LBB0_799:
	s_add_i32 s9, s5, -1
	s_ff1_i32_b32 s8, s5
	s_and_b32 s5, s9, s5
	v_sub_co_u32_e64 v33, s[14:15], s5, 1
	s_ff1_i32_b32 s9, s5
	s_and_b64 vcc, s[14:15], exec
	s_cselect_b32 s18, s8, s9
	v_readlane_b32 s14, v32, s8
	s_lshl_b32 s8, s8, 4
	s_add_i32 s16, s8, s3
	s_ashr_i32 s17, s16, 31
	s_ashr_i32 s15, s14, 31
	s_lshl_b64 s[16:17], s[16:17], 20
	s_add_u32 s8, s11, s16
	s_addc_u32 s16, s12, s17
	s_lshl_b64 s[14:15], s[14:15], 11
	s_add_u32 s14, s8, s14
	s_addc_u32 s15, s16, s15
	v_lshl_add_u64 v[34:35], v[64:65], 3, s[14:15]
	global_load_dwordx2 v[36:37], v[34:35], off nt
	global_load_dwordx2 v[38:39], v[34:35], off offset:512 nt
	global_load_dwordx2 v[40:41], v[34:35], off offset:1024 nt
	global_load_dwordx2 v[42:43], v[34:35], off offset:1536 nt
	v_readfirstlane_b32 s14, v33
	v_readlane_b32 s8, v32, s18
	s_cbranch_vccnz .Lp8_single
	s_lshl_b32 s9, s9, 4
	s_add_i32 s16, s9, s3
	s_ashr_i32 s17, s16, 31
	s_lshl_b64 s[16:17], s[16:17], 20
	s_add_u32 s15, s11, s16
	s_addc_u32 s16, s12, s17
	s_ashr_i32 s9, s8, 31
	s_lshl_b64 s[8:9], s[8:9], 11
	s_add_u32 s8, s15, s8
	s_addc_u32 s9, s16, s9
	v_lshl_add_u64 v[34:35], v[64:65], 3, s[8:9]
	global_load_dwordx2 v[92:93], v[34:35], off nt
	global_load_dwordx2 v[94:95], v[34:35], off offset:512 nt
	global_load_dwordx2 v[96:97], v[34:35], off offset:1024 nt
	global_load_dwordx2 v[98:99], v[34:35], off offset:1536 nt
	s_waitcnt vmcnt(7)
	v_lshlrev_b32_e32 v34, 16, v36
	v_and_b32_e32 v35, 0xffff0000, v36
	v_lshlrev_b32_e32 v36, 16, v37
	v_and_b32_e32 v37, 0xffff0000, v37
	s_waitcnt vmcnt(6)
	v_lshlrev_b32_e32 v44, 16, v38
	v_and_b32_e32 v45, 0xffff0000, v38
	v_lshlrev_b32_e32 v38, 16, v39
	v_and_b32_e32 v39, 0xffff0000, v39
	s_waitcnt vmcnt(5)
	v_lshlrev_b32_e32 v46, 16, v40
	v_and_b32_e32 v47, 0xffff0000, v40
	v_lshlrev_b32_e32 v40, 16, v41
	v_and_b32_e32 v41, 0xffff0000, v41
	s_waitcnt vmcnt(4)
	v_lshlrev_b32_e32 v90, 16, v42
	v_and_b32_e32 v91, 0xffff0000, v42
	v_lshlrev_b32_e32 v42, 16, v43
	v_and_b32_e32 v43, 0xffff0000, v43
	v_pk_add_f32 v[16:17], v[16:17], v[34:35]
	v_pk_add_f32 v[18:19], v[18:19], v[36:37]
	v_pk_add_f32 v[20:21], v[20:21], v[44:45]
	v_pk_add_f32 v[22:23], v[22:23], v[38:39]
	v_pk_add_f32 v[24:25], v[24:25], v[46:47]
	v_pk_add_f32 v[26:27], v[26:27], v[40:41]
	v_pk_add_f32 v[28:29], v[28:29], v[90:91]
	v_pk_add_f32 v[30:31], v[30:31], v[42:43]
	s_waitcnt vmcnt(3)
	v_lshlrev_b32_e32 v34, 16, v92
	v_and_b32_e32 v35, 0xffff0000, v92
	v_lshlrev_b32_e32 v36, 16, v93
	v_and_b32_e32 v37, 0xffff0000, v93
	s_waitcnt vmcnt(2)
	v_lshlrev_b32_e32 v44, 16, v94
	v_and_b32_e32 v45, 0xffff0000, v94
	v_lshlrev_b32_e32 v38, 16, v95
	v_and_b32_e32 v39, 0xffff0000, v95
	s_waitcnt vmcnt(1)
	v_lshlrev_b32_e32 v46, 16, v96
	v_and_b32_e32 v47, 0xffff0000, v96
	v_lshlrev_b32_e32 v40, 16, v97
	v_and_b32_e32 v41, 0xffff0000, v97
	s_waitcnt vmcnt(0)
	v_lshlrev_b32_e32 v90, 16, v98
	v_and_b32_e32 v91, 0xffff0000, v98
	v_lshlrev_b32_e32 v42, 16, v99
	v_and_b32_e32 v43, 0xffff0000, v99
	v_pk_add_f32 v[16:17], v[16:17], v[34:35]
	v_pk_add_f32 v[18:19], v[18:19], v[36:37]
	v_pk_add_f32 v[20:21], v[20:21], v[44:45]
	v_pk_add_f32 v[22:23], v[22:23], v[38:39]
	v_pk_add_f32 v[24:25], v[24:25], v[46:47]
	v_pk_add_f32 v[26:27], v[26:27], v[40:41]
	v_pk_add_f32 v[28:29], v[28:29], v[90:91]
	v_pk_add_f32 v[30:31], v[30:31], v[42:43]
	s_branch .LBB0_798
.Lp8_single:
	s_waitcnt vmcnt(3)
	v_lshlrev_b32_e32 v34, 16, v36
	v_and_b32_e32 v35, 0xffff0000, v36
	v_lshlrev_b32_e32 v36, 16, v37
	v_and_b32_e32 v37, 0xffff0000, v37
	s_waitcnt vmcnt(2)
	v_lshlrev_b32_e32 v44, 16, v38
	v_and_b32_e32 v45, 0xffff0000, v38
	v_lshlrev_b32_e32 v38, 16, v39
	v_and_b32_e32 v39, 0xffff0000, v39
	s_waitcnt vmcnt(1)
	v_lshlrev_b32_e32 v46, 16, v40
	v_and_b32_e32 v47, 0xffff0000, v40
	v_lshlrev_b32_e32 v40, 16, v41
	v_and_b32_e32 v41, 0xffff0000, v41
	s_waitcnt vmcnt(0)
	v_lshlrev_b32_e32 v90, 16, v42
	v_and_b32_e32 v91, 0xffff0000, v42
	v_lshlrev_b32_e32 v42, 16, v43
	v_and_b32_e32 v43, 0xffff0000, v43
	v_pk_add_f32 v[16:17], v[16:17], v[34:35]
	v_pk_add_f32 v[18:19], v[18:19], v[36:37]
	v_pk_add_f32 v[20:21], v[20:21], v[44:45]
	v_pk_add_f32 v[22:23], v[22:23], v[38:39]
	v_pk_add_f32 v[24:25], v[24:25], v[46:47]
	v_pk_add_f32 v[26:27], v[26:27], v[40:41]
	v_pk_add_f32 v[28:29], v[28:29], v[90:91]
	v_pk_add_f32 v[30:31], v[30:31], v[42:43]
	s_branch .LBB0_798
